# in-proj GEMM K-loop: s_setprio 1/0 toggles around the MFMA clusters removed
# baseline (speedup 1.0000x reference)
; #define G_STAGE2(bufoff, gbase, v0, v1) do { \
;         __builtin_amdgcn_global_load_lds((const unsigned*)((const char*)(gbase) + (v0)), (LAS unsigned*)(lds + (bufoff) + ldsw), 16, 0, 0); \
;         __builtin_amdgcn_global_load_lds((const unsigned*)((const char*)(gbase) + (v1)), (LAS unsigned*)(lds + (bufoff) + ldsw + 8192), 16, 0, 0); } while (0)
; #define G_WAIT_V(n) asm volatile("s_waitcnt vmcnt(" #n ")" ::: "memory")
; #define G_BAR __builtin_amdgcn_s_barrier()
; template <bool PERM, class Epi, class Sched>
; __device__ __forceinline__ void gemm_phase(LAS unsigned char* lds, const Sched& S, const Epi& E) {
;     ...
;         for (int t = 0; t < nt; t += 2) {
;             const bool last = (t == nt - 2);
;             const char* a1 = cA + (size_t)(t + 1) * kstep;
;             G_LDB(B0, 0, 0); G_SCHED; G_LDA(At, 0, 0); G_STAGE2(G_SA(1, 1), a1, va10, va11);
;             const char* a2 = last ? nA : cA + (size_t)(t + 2) * kstep; const char* b2 = last ? nB : cB + (size_t)(t + 2) * kstep;
;             if (last) {
;                 if (Sched::GATHER_A) { va00 = na00; va01 = na01; va10 = na10; va11 = na11; vb0 = nb0; vb1 = nb1; hsB = nhsB; }
;                 else if (has_next) G_OFFS(nxt, va00, va01, va10, va11, vb0, vb1, hsB);
;             }
;             const char* a3 = a2 + kstep; const char* b3 = b2 + kstep;
;             G_WAIT_L(8); G_BAR; G_WAIT_L(0); G_MMA(0, 0, At, B0); G_BAR; G_SCHED;
;             G_LDB(B1, 0, 1); G_STAGE2(G_SB(0, 0), b2, vb0, vb1);
;             G_BAR; G_WAIT_L(0); G_MMA(0, 1, At, B1); G_BAR;
;             G_LDA(At, 0, 1); G_STAGE2(G_SA(0, 0), a2, va00, va01);
;             G_BAR; G_WAIT_L(0); G_MMA(1, 0, At, B0); G_BAR; G_SCHED;
;             G_STAGE2(G_SB(0, 1), b2 + hsB, vb0, vb1);
;             G_WAIT_V(6); G_BAR; G_MMA(1, 1, At, B1); G_BAR;
;             G_LDB(B0, 1, 0); G_SCHED; G_LDA(At, 1, 0); G_STAGE2(G_SA(0, 1), a2, va10, va11);
;             G_WAIT_L(8); G_BAR; G_WAIT_L(0); G_MMA(0, 0, At, B0); G_BAR; G_SCHED;
;             G_LDB(B1, 1, 1); G_STAGE2(G_SB(1, 0), b3, vb0, vb1);
;             G_BAR; G_WAIT_L(0); G_MMA(0, 1, At, B1); G_BAR;
;             G_LDA(At, 1, 1); G_STAGE2(G_SA(1, 0), a3, va00, va01);
;             G_BAR; G_WAIT_L(0); G_MMA(1, 0, At, B0); G_BAR; G_SCHED;
;             G_STAGE2(G_SB(1, 1), b3 + hsB, vb0, vb1);
;             G_WAIT_V(6); G_BAR; G_MMA(1, 1, At, B1); G_BAR;
.LBB0_253:
	s_add_u32 s18, s28, 0x80
	s_waitcnt lgkmcnt(8)
	s_barrier
	s_waitcnt lgkmcnt(0)
	s_addc_u32 s19, s29, 0
	s_and_b64 s[8:9], s[8:9], exec
	v_mov_b32_e32 v205, v147
	v_mov_b32_e32 v207, v147
	s_cselect_b32 s19, s69, s19
	s_cselect_b32 s18, s68, s18
	s_cselect_b32 s9, s71, s2
	s_cselect_b32 s8, s70, s1
	s_waitcnt lgkmcnt(0)
	v_mfma_f32_16x16x32_bf16 v[126:129], v[130:133], v[172:175], v[126:129]
	v_mfma_f32_16x16x32_bf16 v[122:125], v[138:141], v[172:175], v[122:125]
	v_mfma_f32_16x16x32_bf16 v[118:121], v[130:133], v[164:167], v[118:121]
	v_mfma_f32_16x16x32_bf16 v[114:117], v[138:141], v[164:167], v[114:117]
	v_mfma_f32_16x16x32_bf16 v[110:113], v[130:133], v[156:159], v[110:113]
	v_mfma_f32_16x16x32_bf16 v[106:109], v[138:141], v[156:159], v[106:109]
	v_mfma_f32_16x16x32_bf16 v[102:105], v[130:133], v[148:151], v[102:105]
	v_mfma_f32_16x16x32_bf16 v[98:101], v[138:141], v[148:151], v[98:101]
	v_mfma_f32_16x16x32_bf16 v[126:129], v[134:137], v[176:179], v[126:129]
	v_mfma_f32_16x16x32_bf16 v[122:125], v[142:145], v[176:179], v[122:125]
	v_mfma_f32_16x16x32_bf16 v[118:121], v[134:137], v[168:171], v[118:121]
	v_mfma_f32_16x16x32_bf16 v[114:117], v[142:145], v[168:171], v[114:117]
	v_mfma_f32_16x16x32_bf16 v[110:113], v[134:137], v[160:163], v[110:113]
	v_mfma_f32_16x16x32_bf16 v[106:109], v[142:145], v[160:163], v[106:109]
	v_mfma_f32_16x16x32_bf16 v[102:105], v[134:137], v[152:155], v[102:105]
	v_mfma_f32_16x16x32_bf16 v[98:101], v[142:145], v[152:155], v[98:101]
	s_barrier
	s_add_i32 s24, 0, 0x14000
	s_mov_b32 m0, s65
	v_add_u32_e32 v192, s24, v1
	ds_read_b128 v[180:183], v192
	ds_read_b128 v[184:187], v192 offset:1024
	ds_read_b128 v[188:191], v192 offset:2048
	ds_read_b128 v[192:195], v192 offset:3072
	global_load_lds_dwordx4 v146, s[8:9]
	s_mov_b32 m0, s73
	v_mov_b32_e32 v209, v147
	global_load_lds_dwordx4 v208, s[8:9]
	s_barrier
	s_waitcnt lgkmcnt(0)
	v_lshl_add_u64 v[210:211], s[8:9], 0, v[146:147]
	v_lshl_add_u64 v[212:213], s[8:9], 0, v[208:209]
	s_waitcnt lgkmcnt(0)
	v_mfma_f32_16x16x32_bf16 v[62:65], v[180:183], v[172:175], v[62:65]
	v_mfma_f32_16x16x32_bf16 v[58:61], v[188:191], v[172:175], v[58:61]
	v_mfma_f32_16x16x32_bf16 v[54:57], v[180:183], v[164:167], v[54:57]
	v_mfma_f32_16x16x32_bf16 v[50:53], v[188:191], v[164:167], v[50:53]
	v_mfma_f32_16x16x32_bf16 v[46:49], v[180:183], v[156:159], v[46:49]
	v_mfma_f32_16x16x32_bf16 v[42:45], v[188:191], v[156:159], v[42:45]
	v_mfma_f32_16x16x32_bf16 v[38:41], v[180:183], v[148:151], v[38:41]
	v_mfma_f32_16x16x32_bf16 v[34:37], v[188:191], v[148:151], v[34:37]
	v_mfma_f32_16x16x32_bf16 v[62:65], v[184:187], v[176:179], v[62:65]
	v_mfma_f32_16x16x32_bf16 v[58:61], v[192:195], v[176:179], v[58:61]
	v_mfma_f32_16x16x32_bf16 v[54:57], v[184:187], v[168:171], v[54:57]
	v_mfma_f32_16x16x32_bf16 v[50:53], v[192:195], v[168:171], v[50:53]
	v_mfma_f32_16x16x32_bf16 v[46:49], v[184:187], v[160:163], v[46:49]
	v_mfma_f32_16x16x32_bf16 v[42:45], v[192:195], v[160:163], v[42:45]
	v_mfma_f32_16x16x32_bf16 v[38:41], v[184:187], v[152:155], v[38:41]
	v_mfma_f32_16x16x32_bf16 v[34:37], v[192:195], v[152:155], v[34:37]
	s_mov_b32 m0, s64
	s_barrier
	ds_read_b128 v[148:151], v199 offset:16384
	ds_read_b128 v[152:155], v199 offset:17408
	ds_read_b128 v[156:159], v199 offset:18432
	ds_read_b128 v[160:163], v199 offset:19456
	ds_read_b128 v[164:167], v199 offset:20480
	ds_read_b128 v[168:171], v199 offset:21504
	ds_read_b128 v[172:175], v199 offset:22528
	ds_read_b128 v[176:179], v199 offset:23552
	global_load_lds_dwordx4 v200, s[18:19]
	s_mov_b32 m0, s75
	v_mov_b32_e32 v201, v147
	global_load_lds_dwordx4 v202, s[18:19]
	s_barrier
	s_waitcnt lgkmcnt(0)
	v_mov_b32_e32 v203, v147
	v_lshl_add_u64 v[214:215], s[18:19], 0, v[200:201]
	v_lshl_add_u64 v[216:217], s[18:19], 0, v[202:203]
	s_waitcnt lgkmcnt(0)
	v_mfma_f32_16x16x32_bf16 v[94:97], v[130:133], v[148:151], v[94:97]
	v_mfma_f32_16x16x32_bf16 v[90:93], v[138:141], v[148:151], v[90:93]
	v_mfma_f32_16x16x32_bf16 v[86:89], v[130:133], v[156:159], v[86:89]
	v_mfma_f32_16x16x32_bf16 v[82:85], v[138:141], v[156:159], v[82:85]
	v_mfma_f32_16x16x32_bf16 v[78:81], v[130:133], v[164:167], v[78:81]
	v_mfma_f32_16x16x32_bf16 v[74:77], v[138:141], v[164:167], v[74:77]
	v_mfma_f32_16x16x32_bf16 v[70:73], v[130:133], v[172:175], v[70:73]
	v_mfma_f32_16x16x32_bf16 v[66:69], v[138:141], v[172:175], v[66:69]
	v_mfma_f32_16x16x32_bf16 v[94:97], v[134:137], v[152:155], v[94:97]
	v_mfma_f32_16x16x32_bf16 v[90:93], v[142:145], v[152:155], v[90:93]
	v_mfma_f32_16x16x32_bf16 v[86:89], v[134:137], v[160:163], v[86:89]
	v_mfma_f32_16x16x32_bf16 v[82:85], v[142:145], v[160:163], v[82:85]
	v_mfma_f32_16x16x32_bf16 v[78:81], v[134:137], v[168:171], v[78:81]
	v_mfma_f32_16x16x32_bf16 v[74:77], v[142:145], v[168:171], v[74:77]
	v_mfma_f32_16x16x32_bf16 v[70:73], v[134:137], v[176:179], v[70:73]
	v_mfma_f32_16x16x32_bf16 v[66:69], v[142:145], v[176:179], v[66:69]
	s_barrier
	s_add_u32 s22, s8, 0x40000
	s_addc_u32 s23, s9, 0
	s_add_i32 s24, s24, s63
	s_mov_b32 m0, s24
	s_nop 0
	global_load_lds_dwordx4 v146, s[22:23]
	s_add_i32 m0, s24, 0x2000
	s_nop 0
	global_load_lds_dwordx4 v208, s[22:23]
	s_waitcnt vmcnt(6)
	s_barrier
; #define G_STAGE2(bufoff, gbase, v0, v1) do { \
;         __builtin_amdgcn_global_load_lds((const unsigned*)((const char*)(gbase) + (v0)), (LAS unsigned*)(lds + (bufoff) + ldsw), 16, 0, 0); \
;         __builtin_amdgcn_global_load_lds((const unsigned*)((const char*)(gbase) + (v1)), (LAS unsigned*)(lds + (bufoff) + ldsw + 8192), 16, 0, 0); } while (0)
; #define G_WAIT_V(n) asm volatile("s_waitcnt vmcnt(" #n ")" ::: "memory")
; #define G_BAR __builtin_amdgcn_s_barrier()
; template <bool PERM, class Epi, class Sched>
; __device__ __forceinline__ void gemm_phase(LAS unsigned char* lds, const Sched& S, const Epi& E) {
;     ...
;         for (int t = 0; t < nt; t += 2) {
;             const bool last = (t == nt - 2);
;             const char* a1 = cA + (size_t)(t + 1) * kstep;
;             G_LDB(B0, 0, 0); G_SCHED; G_LDA(At, 0, 0); G_STAGE2(G_SA(1, 1), a1, va10, va11);
;             const char* a2 = last ? nA : cA + (size_t)(t + 2) * kstep; const char* b2 = last ? nB : cB + (size_t)(t + 2) * kstep;
;             if (last) {
;                 if (Sched::GATHER_A) { va00 = na00; va01 = na01; va10 = na10; va11 = na11; vb0 = nb0; vb1 = nb1; hsB = nhsB; }
;                 else if (has_next) G_OFFS(nxt, va00, va01, va10, va11, vb0, vb1, hsB);
;             }
;             const char* a3 = a2 + kstep; const char* b3 = b2 + kstep;
;             G_WAIT_L(8); G_BAR; G_WAIT_L(0); G_MMA(0, 0, At, B0); G_BAR; G_SCHED;
;             G_LDB(B1, 0, 1); G_STAGE2(G_SB(0, 0), b2, vb0, vb1);
;             G_BAR; G_WAIT_L(0); G_MMA(0, 1, At, B1); G_BAR;
;             G_LDA(At, 0, 1); G_STAGE2(G_SA(0, 0), a2, va00, va01);
;             G_BAR; G_WAIT_L(0); G_MMA(1, 0, At, B0); G_BAR; G_SCHED;
;             G_STAGE2(G_SB(0, 1), b2 + hsB, vb0, vb1);
;             G_WAIT_V(6); G_BAR; G_MMA(1, 1, At, B1); G_BAR;
;             G_LDB(B0, 1, 0); G_SCHED; G_LDA(At, 1, 0); G_STAGE2(G_SA(0, 1), a2, va10, va11);
;             G_WAIT_L(8); G_BAR; G_WAIT_L(0); G_MMA(0, 0, At, B0); G_BAR; G_SCHED;
;             G_LDB(B1, 1, 1); G_STAGE2(G_SB(1, 0), b3, vb0, vb1);
;             G_BAR; G_WAIT_L(0); G_MMA(0, 1, At, B1); G_BAR;
;             G_LDA(At, 1, 1); G_STAGE2(G_SA(1, 0), a3, va00, va01);
;             G_BAR; G_WAIT_L(0); G_MMA(1, 0, At, B0); G_BAR; G_SCHED;
;             G_STAGE2(G_SB(1, 1), b3 + hsB, vb0, vb1);
;             G_WAIT_V(6); G_BAR; G_MMA(1, 1, At, B1); G_BAR;
	v_mfma_f32_16x16x32_bf16 v[30:33], v[180:183], v[148:151], v[30:33]
	v_mfma_f32_16x16x32_bf16 v[26:29], v[188:191], v[148:151], v[26:29]
	v_mfma_f32_16x16x32_bf16 v[22:25], v[180:183], v[156:159], v[22:25]
	v_mfma_f32_16x16x32_bf16 v[18:21], v[188:191], v[156:159], v[18:21]
	v_mfma_f32_16x16x32_bf16 v[14:17], v[180:183], v[164:167], v[14:17]
	v_mfma_f32_16x16x32_bf16 v[10:13], v[188:191], v[164:167], v[10:13]
	v_mfma_f32_16x16x32_bf16 v[6:9], v[180:183], v[172:175], v[6:9]
	v_mfma_f32_16x16x32_bf16 v[2:5], v[188:191], v[172:175], v[2:5]
	v_mfma_f32_16x16x32_bf16 v[30:33], v[184:187], v[152:155], v[30:33]
	v_mfma_f32_16x16x32_bf16 v[26:29], v[192:195], v[152:155], v[26:29]
	v_mfma_f32_16x16x32_bf16 v[22:25], v[184:187], v[160:163], v[22:25]
	v_mfma_f32_16x16x32_bf16 v[18:21], v[192:195], v[160:163], v[18:21]
	v_mfma_f32_16x16x32_bf16 v[14:17], v[184:187], v[168:171], v[14:17]
	v_mfma_f32_16x16x32_bf16 v[10:13], v[192:195], v[168:171], v[10:13]
	v_mfma_f32_16x16x32_bf16 v[6:9], v[184:187], v[176:179], v[6:9]
	v_mfma_f32_16x16x32_bf16 v[2:5], v[192:195], v[176:179], v[2:5]
	s_add_i32 s22, 0, 0x18000
	v_add_u32_e32 v142, s22, v1
	s_barrier
	ds_read_b128 v[130:133], v142
	ds_read_b128 v[134:137], v142 offset:1024
	ds_read_b128 v[138:141], v142 offset:2048
	ds_read_b128 v[142:145], v142 offset:3072
	s_mov_b32 m0, s80
	v_lshl_add_u64 v[180:181], s[18:19], 0, v[204:205]
	ds_read_b128 v[148:151], v199 offset:32768
	ds_read_b128 v[152:155], v199 offset:33792
	ds_read_b128 v[156:159], v199 offset:34816
	ds_read_b128 v[160:163], v199 offset:35840
	ds_read_b128 v[164:167], v199 offset:36864
	ds_read_b128 v[168:171], v199 offset:37888
	ds_read_b128 v[172:175], v199 offset:38912
	ds_read_b128 v[176:179], v199 offset:39936
	global_load_lds_dwordx4 v[180:181], off
	v_lshl_add_u64 v[180:181], s[18:19], 0, v[206:207]
	s_mov_b32 m0, s81
	s_nop 0
	global_load_lds_dwordx4 v[180:181], off
	s_waitcnt lgkmcnt(8)
	s_barrier
	s_waitcnt lgkmcnt(0)
	s_waitcnt lgkmcnt(0)
	v_mfma_f32_16x16x32_bf16 v[126:129], v[130:133], v[148:151], v[126:129]
	v_mfma_f32_16x16x32_bf16 v[122:125], v[138:141], v[148:151], v[122:125]
	v_mfma_f32_16x16x32_bf16 v[118:121], v[130:133], v[156:159], v[118:121]
	v_mfma_f32_16x16x32_bf16 v[114:117], v[138:141], v[156:159], v[114:117]
	v_mfma_f32_16x16x32_bf16 v[110:113], v[130:133], v[164:167], v[110:113]
	v_mfma_f32_16x16x32_bf16 v[106:109], v[138:141], v[164:167], v[106:109]
	v_mfma_f32_16x16x32_bf16 v[102:105], v[130:133], v[172:175], v[102:105]
	v_mfma_f32_16x16x32_bf16 v[98:101], v[138:141], v[172:175], v[98:101]
	v_mfma_f32_16x16x32_bf16 v[126:129], v[134:137], v[152:155], v[126:129]
	v_mfma_f32_16x16x32_bf16 v[122:125], v[142:145], v[152:155], v[122:125]
	v_mfma_f32_16x16x32_bf16 v[118:121], v[134:137], v[160:163], v[118:121]
	v_mfma_f32_16x16x32_bf16 v[114:117], v[142:145], v[160:163], v[114:117]
	v_mfma_f32_16x16x32_bf16 v[110:113], v[134:137], v[168:171], v[110:113]
	v_mfma_f32_16x16x32_bf16 v[106:109], v[142:145], v[168:171], v[106:109]
	v_mfma_f32_16x16x32_bf16 v[102:105], v[134:137], v[176:179], v[102:105]
	v_mfma_f32_16x16x32_bf16 v[98:101], v[142:145], v[176:179], v[98:101]
	s_barrier
	s_add_i32 s18, 0, 0x1c000
	s_add_i32 s19, s22, s63
	v_add_u32_e32 v192, s18, v1
	v_lshl_add_u64 v[210:211], v[210:211], 0, s[34:35]
	s_mov_b32 m0, s19
	ds_read_b128 v[180:183], v192
	ds_read_b128 v[184:187], v192 offset:1024
	ds_read_b128 v[188:191], v192 offset:2048
	ds_read_b128 v[192:195], v192 offset:3072
	global_load_lds_dwordx4 v[210:211], off
	v_lshl_add_u64 v[210:211], v[212:213], 0, s[34:35]
	s_add_i32 m0, s19, 0x2000
	s_nop 0
	global_load_lds_dwordx4 v[210:211], off
	s_barrier
; #define G_STAGE2(bufoff, gbase, v0, v1) do { \
;         __builtin_amdgcn_global_load_lds((const unsigned*)((const char*)(gbase) + (v0)), (LAS unsigned*)(lds + (bufoff) + ldsw), 16, 0, 0); \
;         __builtin_amdgcn_global_load_lds((const unsigned*)((const char*)(gbase) + (v1)), (LAS unsigned*)(lds + (bufoff) + ldsw + 8192), 16, 0, 0); } while (0)
; #define G_WAIT_V(n) asm volatile("s_waitcnt vmcnt(" #n ")" ::: "memory")
; #define G_BAR __builtin_amdgcn_s_barrier()
; template <bool PERM, class Epi, class Sched>
; __device__ __forceinline__ void gemm_phase(LAS unsigned char* lds, const Sched& S, const Epi& E) {
;     ...
;         for (int t = 0; t < nt; t += 2) {
;             const bool last = (t == nt - 2);
;             const char* a1 = cA + (size_t)(t + 1) * kstep;
;             G_LDB(B0, 0, 0); G_SCHED; G_LDA(At, 0, 0); G_STAGE2(G_SA(1, 1), a1, va10, va11);
;             const char* a2 = last ? nA : cA + (size_t)(t + 2) * kstep; const char* b2 = last ? nB : cB + (size_t)(t + 2) * kstep;
;             if (last) {
;                 if (Sched::GATHER_A) { va00 = na00; va01 = na01; va10 = na10; va11 = na11; vb0 = nb0; vb1 = nb1; hsB = nhsB; }
;                 else if (has_next) G_OFFS(nxt, va00, va01, va10, va11, vb0, vb1, hsB);
;             }
;             const char* a3 = a2 + kstep; const char* b3 = b2 + kstep;
;             G_WAIT_L(8); G_BAR; G_WAIT_L(0); G_MMA(0, 0, At, B0); G_BAR; G_SCHED;
;             G_LDB(B1, 0, 1); G_STAGE2(G_SB(0, 0), b2, vb0, vb1);
;             G_BAR; G_WAIT_L(0); G_MMA(0, 1, At, B1); G_BAR;
;             G_LDA(At, 0, 1); G_STAGE2(G_SA(0, 0), a2, va00, va01);
;             G_BAR; G_WAIT_L(0); G_MMA(1, 0, At, B0); G_BAR; G_SCHED;
;             G_STAGE2(G_SB(0, 1), b2 + hsB, vb0, vb1);
;             G_WAIT_V(6); G_BAR; G_MMA(1, 1, At, B1); G_BAR;
;             G_LDB(B0, 1, 0); G_SCHED; G_LDA(At, 1, 0); G_STAGE2(G_SA(0, 1), a2, va10, va11);
;             G_WAIT_L(8); G_BAR; G_WAIT_L(0); G_MMA(0, 0, At, B0); G_BAR; G_SCHED;
;             G_LDB(B1, 1, 1); G_STAGE2(G_SB(1, 0), b3, vb0, vb1);
;             G_BAR; G_WAIT_L(0); G_MMA(0, 1, At, B1); G_BAR;
;             G_LDA(At, 1, 1); G_STAGE2(G_SA(1, 0), a3, va00, va01);
;             G_BAR; G_WAIT_L(0); G_MMA(1, 0, At, B0); G_BAR; G_SCHED;
;             G_STAGE2(G_SB(1, 1), b3 + hsB, vb0, vb1);
;             G_WAIT_V(6); G_BAR; G_MMA(1, 1, At, B1); G_BAR;
	s_waitcnt lgkmcnt(0)
	s_waitcnt lgkmcnt(0)
	v_mfma_f32_16x16x32_bf16 v[62:65], v[180:183], v[148:151], v[62:65]
	v_mfma_f32_16x16x32_bf16 v[58:61], v[188:191], v[148:151], v[58:61]
	v_mfma_f32_16x16x32_bf16 v[54:57], v[180:183], v[156:159], v[54:57]
	v_mfma_f32_16x16x32_bf16 v[50:53], v[188:191], v[156:159], v[50:53]
	v_mfma_f32_16x16x32_bf16 v[46:49], v[180:183], v[164:167], v[46:49]
	v_mfma_f32_16x16x32_bf16 v[42:45], v[188:191], v[164:167], v[42:45]
	v_mfma_f32_16x16x32_bf16 v[38:41], v[180:183], v[172:175], v[38:41]
	v_mfma_f32_16x16x32_bf16 v[34:37], v[188:191], v[172:175], v[34:37]
	v_mfma_f32_16x16x32_bf16 v[62:65], v[184:187], v[152:155], v[62:65]
	v_mfma_f32_16x16x32_bf16 v[58:61], v[192:195], v[152:155], v[58:61]
	v_mfma_f32_16x16x32_bf16 v[54:57], v[184:187], v[160:163], v[54:57]
	v_mfma_f32_16x16x32_bf16 v[50:53], v[192:195], v[160:163], v[50:53]
	v_mfma_f32_16x16x32_bf16 v[46:49], v[184:187], v[168:171], v[46:49]
	v_mfma_f32_16x16x32_bf16 v[42:45], v[192:195], v[168:171], v[42:45]
	v_mfma_f32_16x16x32_bf16 v[38:41], v[184:187], v[176:179], v[38:41]
	v_mfma_f32_16x16x32_bf16 v[34:37], v[192:195], v[176:179], v[34:37]
	s_mov_b32 m0, s83
	v_lshl_add_u64 v[210:211], v[214:215], 0, s[34:35]
	s_barrier
	ds_read_b128 v[148:151], v199 offset:49152
	ds_read_b128 v[152:155], v199 offset:50176
	ds_read_b128 v[156:159], v199 offset:51200
	ds_read_b128 v[160:163], v199 offset:52224
	ds_read_b128 v[164:167], v199 offset:53248
	ds_read_b128 v[168:171], v199 offset:54272
	ds_read_b128 v[172:175], v199 offset:55296
	ds_read_b128 v[176:179], v199 offset:56320
	global_load_lds_dwordx4 v[210:211], off
	v_lshl_add_u64 v[210:211], v[216:217], 0, s[34:35]
	s_mov_b32 m0, s84
	s_nop 0
	global_load_lds_dwordx4 v[210:211], off
	s_barrier
	s_waitcnt lgkmcnt(0)
	s_waitcnt lgkmcnt(0)
	v_mfma_f32_16x16x32_bf16 v[94:97], v[130:133], v[148:151], v[94:97]
	v_mfma_f32_16x16x32_bf16 v[90:93], v[138:141], v[148:151], v[90:93]
	v_mfma_f32_16x16x32_bf16 v[86:89], v[130:133], v[156:159], v[86:89]
	v_mfma_f32_16x16x32_bf16 v[82:85], v[138:141], v[156:159], v[82:85]
	v_mfma_f32_16x16x32_bf16 v[78:81], v[130:133], v[164:167], v[78:81]
	v_mfma_f32_16x16x32_bf16 v[74:77], v[138:141], v[164:167], v[74:77]
	v_mfma_f32_16x16x32_bf16 v[70:73], v[130:133], v[172:175], v[70:73]
	v_mfma_f32_16x16x32_bf16 v[66:69], v[138:141], v[172:175], v[66:69]
	v_mfma_f32_16x16x32_bf16 v[94:97], v[134:137], v[152:155], v[94:97]
	v_mfma_f32_16x16x32_bf16 v[90:93], v[142:145], v[152:155], v[90:93]
	v_mfma_f32_16x16x32_bf16 v[86:89], v[134:137], v[160:163], v[86:89]
	v_mfma_f32_16x16x32_bf16 v[82:85], v[142:145], v[160:163], v[82:85]
	v_mfma_f32_16x16x32_bf16 v[78:81], v[134:137], v[168:171], v[78:81]
	v_mfma_f32_16x16x32_bf16 v[74:77], v[142:145], v[168:171], v[74:77]
	v_mfma_f32_16x16x32_bf16 v[70:73], v[134:137], v[176:179], v[70:73]
	v_mfma_f32_16x16x32_bf16 v[66:69], v[142:145], v[176:179], v[66:69]
	s_barrier
	s_add_u32 s8, s8, 0x40080
	s_addc_u32 s9, s9, 0
	s_add_i32 s18, s18, s63
	s_mov_b32 m0, s18
	s_nop 0
	global_load_lds_dwordx4 v146, s[8:9]
	s_add_i32 m0, s18, 0x2000
	s_nop 0
	global_load_lds_dwordx4 v208, s[8:9]
	s_waitcnt vmcnt(6)
	s_barrier
	v_mfma_f32_16x16x32_bf16 v[30:33], v[180:183], v[148:151], v[30:33]
	v_mfma_f32_16x16x32_bf16 v[26:29], v[188:191], v[148:151], v[26:29]
	v_mfma_f32_16x16x32_bf16 v[22:25], v[180:183], v[156:159], v[22:25]
	v_mfma_f32_16x16x32_bf16 v[18:21], v[188:191], v[156:159], v[18:21]
	v_mfma_f32_16x16x32_bf16 v[14:17], v[180:183], v[164:167], v[14:17]
	v_mfma_f32_16x16x32_bf16 v[10:13], v[188:191], v[164:167], v[10:13]
	v_mfma_f32_16x16x32_bf16 v[6:9], v[180:183], v[172:175], v[6:9]
	v_mfma_f32_16x16x32_bf16 v[2:5], v[188:191], v[172:175], v[2:5]
	v_mfma_f32_16x16x32_bf16 v[30:33], v[184:187], v[152:155], v[30:33]
	v_mfma_f32_16x16x32_bf16 v[26:29], v[192:195], v[152:155], v[26:29]
	v_mfma_f32_16x16x32_bf16 v[22:25], v[184:187], v[160:163], v[22:25]
	v_mfma_f32_16x16x32_bf16 v[18:21], v[192:195], v[160:163], v[18:21]
	v_mfma_f32_16x16x32_bf16 v[14:17], v[184:187], v[168:171], v[14:17]
	v_mfma_f32_16x16x32_bf16 v[10:13], v[192:195], v[168:171], v[10:13]
	v_mfma_f32_16x16x32_bf16 v[6:9], v[184:187], v[176:179], v[6:9]
	v_mfma_f32_16x16x32_bf16 v[2:5], v[192:195], v[176:179], v[2:5]
	s_add_i32 s7, s7, 2
	s_add_u32 s28, s28, 0x100
	s_addc_u32 s29, s29, 0
	s_add_u32 s1, s1, 0x100
	s_addc_u32 s2, s2, 0
	s_cmp_gt_u32 s7, 13
	s_barrier
	s_cbranch_scc1 .LBB0_256
